# prologue de-serialisation: conv-front depthwise-weight copy to LDS as 31 loads + one wait + 31 ds_write instead of a 16-round-trip load/wait/write ladder
# speedup vs baseline: 1.0088x; 1.0081x over previous
; #define LAS __attribute__((address_space(3)))
; #define INL(off) (INR(pb + (off)) && !((PH_DIS >> (1 + (off))) & 1) && (!probe_ || ((PROBE_COLD >> (off)) & 1)))
; #define LAUNDER MKCTX; asm volatile("" : "+v"(C.tid), "+v"(C.lane), "+v"(C.gtid)); asm volatile("" : "+s"(C.blk), "+s"(C.vcu), "+s"(C.gw)); PTRS
; __device__ __forceinline__ void convpre_phase(const Ctx& C, const bf16* Z, const float* dw_w, const float* dw_b, const float* ln_g, const float* ln_b, bf16* ZC) {
;     const __amdgpu_buffer_rsrc_t zrs = __builtin_amdgcn_make_buffer_rsrc((void*)ZC, (short)0, T * CONV_CH * 2, 0x00020000);
;     LAS float* wl = (LAS float*)(C.lds + RING_OFF);
;     LAS bf16* zs = (LAS bf16*)(C.lds + RING_OFF + 63488);
;     __syncthreads();
;     for (int i = C.tid; i < CONV_W * CONV_CH; i += 512) wl[i] = dw_w[i];
; __global__ void __launch_bounds__(512, 2) mega_fwd(Args args) {
;     ...
;         if (INL(2)) for (int rep_ = 0; rep_ < NREP(3); ++rep_) { LAUNDER;
;             unsigned* zc_cnt = (unsigned*)(ws + WS_CTL) + CW_ZC + 64 * l + 2048 * rep_ + (probe_ ? 4096 : 0);
;             convpre_phase(C, Zb, GIN(4) + l * CONV_W * CONV_CH, GIN(5) + l * CONV_CH, GIN(6) + l * CONV_CH, GIN(7) + l * CONV_CH, ZC);
.LBB0_461:
	v_readlane_b32 s0, v254, 20
	s_mul_i32 s0, s0, 10
	v_readlane_b32 s8, v253, 8
	s_add_i32 s2, s0, 3
	v_readlane_b32 s12, v253, 12
	v_readlane_b32 s1, v254, 21
	v_readlane_b32 s13, v253, 13
	s_cmp_le_i32 s12, s2
	s_cselect_b64 s[0:1], -1, 0
	s_cmp_lt_i32 s2, s13
	s_cselect_b64 s[2:3], -1, 0
	s_and_b64 s[0:1], s[0:1], s[2:3]
	v_writelane_b32 v254, s0, 23
	v_readlane_b32 s10, v253, 10
	v_readlane_b32 s11, v253, 11
	v_writelane_b32 v254, s1, 24
	s_andn2_b64 vcc, exec, s[0:1]
	v_readlane_b32 s9, v253, 9
	v_readlane_b32 s14, v253, 14
	v_readlane_b32 s15, v253, 15
	s_cbranch_vccnz .LBB0_665
	v_readlane_b32 s0, v253, 16
	v_mbcnt_lo_u32_b32 v218, -1, 0
	v_mbcnt_hi_u32_b32 v218, -1, v218
	v_readlane_b32 s2, v253, 17
	s_mov_b64 s[4:5], s[10:11]
	v_add_u32_e32 v202, s0, v218
	v_readlane_b32 s0, v253, 19
	v_readlane_b32 s12, v253, 1
	v_readlane_b32 s13, v253, 2
	v_add_u32_e32 v219, s0, v202
	v_readlane_b32 s0, v253, 0
	s_mov_b32 s1, s0
	v_readlane_b32 s0, v253, 18
	s_nop 0
	v_writelane_b32 v254, s2, 25
	v_writelane_b32 v254, s1, 26
	s_nop 0
	v_readlane_b32 s0, v254, 3
	v_readlane_b32 s1, v254, 4
	v_readlane_b32 s2, v254, 5
	v_readlane_b32 s3, v254, 6
	s_add_u32 s0, s4, 0x41000000
	v_writelane_b32 v254, s0, 3
	s_nop 1
	v_writelane_b32 v254, s1, 4
	v_writelane_b32 v254, s2, 5
	v_writelane_b32 v254, s3, 6
	v_writelane_b32 v254, s4, 27
	s_addc_u32 s0, s5, 0
	s_nop 0
	v_writelane_b32 v254, s5, 28
	v_writelane_b32 v254, s0, 29
	v_writelane_b32 v254, s12, 30
	s_load_dwordx8 s[4:11], s[12:13], 0x20
	s_movk_i32 s0, 0x3e00
	v_writelane_b32 v254, s13, 31
	v_cmp_gt_i32_e32 vcc, s0, v202
	s_waitcnt vmcnt(0) lgkmcnt(0)
	s_barrier
	s_and_saveexec_b64 s[0:1], vcc
	s_cbranch_execz .LBB0_475
	v_readlane_b32 s12, v254, 20
	v_lshlrev_b32_e32 v0, 2, v202
	s_mul_i32 s30, s12, 0x3e00
	s_lshl_b64 s[12:13], s[30:31], 2
	s_add_u32 s12, s4, s12
	s_addc_u32 s13, s5, s13
	global_load_dword v4, v0, s[12:13]
	global_load_dword v5, v0, s[12:13] offset:2048
	s_add_u32 s12, s12, 0x1000
	s_addc_u32 s13, s13, 0
	global_load_dword v6, v0, s[12:13]
	global_load_dword v7, v0, s[12:13] offset:2048
	s_add_u32 s12, s12, 0x1000
	s_addc_u32 s13, s13, 0
	global_load_dword v8, v0, s[12:13]
	global_load_dword v9, v0, s[12:13] offset:2048
	s_add_u32 s12, s12, 0x1000
	s_addc_u32 s13, s13, 0
	global_load_dword v10, v0, s[12:13]
	global_load_dword v11, v0, s[12:13] offset:2048
	s_add_u32 s12, s12, 0x1000
	s_addc_u32 s13, s13, 0
	global_load_dword v12, v0, s[12:13]
	global_load_dword v13, v0, s[12:13] offset:2048
	s_add_u32 s12, s12, 0x1000
	s_addc_u32 s13, s13, 0
	global_load_dword v14, v0, s[12:13]
	global_load_dword v15, v0, s[12:13] offset:2048
	s_add_u32 s12, s12, 0x1000
	s_addc_u32 s13, s13, 0
	global_load_dword v16, v0, s[12:13]
	global_load_dword v17, v0, s[12:13] offset:2048
	s_add_u32 s12, s12, 0x1000
	s_addc_u32 s13, s13, 0
	global_load_dword v18, v0, s[12:13]
	global_load_dword v19, v0, s[12:13] offset:2048
	s_add_u32 s12, s12, 0x1000
	s_addc_u32 s13, s13, 0
	global_load_dword v20, v0, s[12:13]
	global_load_dword v21, v0, s[12:13] offset:2048
	s_add_u32 s12, s12, 0x1000
	s_addc_u32 s13, s13, 0
	global_load_dword v22, v0, s[12:13]
	global_load_dword v23, v0, s[12:13] offset:2048
	s_add_u32 s12, s12, 0x1000
	s_addc_u32 s13, s13, 0
	global_load_dword v24, v0, s[12:13]
	global_load_dword v25, v0, s[12:13] offset:2048
	s_add_u32 s12, s12, 0x1000
	s_addc_u32 s13, s13, 0
	global_load_dword v26, v0, s[12:13]
	global_load_dword v27, v0, s[12:13] offset:2048
	s_add_u32 s12, s12, 0x1000
	s_addc_u32 s13, s13, 0
	global_load_dword v28, v0, s[12:13]
	global_load_dword v29, v0, s[12:13] offset:2048
	s_add_u32 s12, s12, 0x1000
	s_addc_u32 s13, s13, 0
	global_load_dword v30, v0, s[12:13]
	global_load_dword v31, v0, s[12:13] offset:2048
	s_add_u32 s12, s12, 0x1000
	s_addc_u32 s13, s13, 0
	global_load_dword v32, v0, s[12:13]
	global_load_dword v33, v0, s[12:13] offset:2048
	s_add_u32 s12, s12, 0x1000
	s_addc_u32 s13, s13, 0
	global_load_dword v34, v0, s[12:13]
	s_waitcnt vmcnt(0)
	ds_write_b32 v0, v4
	ds_write_b32 v0, v5 offset:2048
	ds_write_b32 v0, v6 offset:4096
	ds_write_b32 v0, v7 offset:6144
	ds_write_b32 v0, v8 offset:8192
	ds_write_b32 v0, v9 offset:10240
	ds_write_b32 v0, v10 offset:12288
	ds_write_b32 v0, v11 offset:14336
	ds_write_b32 v0, v12 offset:16384
	ds_write_b32 v0, v13 offset:18432
	ds_write_b32 v0, v14 offset:20480
	ds_write_b32 v0, v15 offset:22528
	ds_write_b32 v0, v16 offset:24576
	ds_write_b32 v0, v17 offset:26624
	ds_write_b32 v0, v18 offset:28672
	ds_write_b32 v0, v19 offset:30720
	ds_write_b32 v0, v20 offset:32768
	ds_write_b32 v0, v21 offset:34816
	ds_write_b32 v0, v22 offset:36864
	ds_write_b32 v0, v23 offset:38912
	ds_write_b32 v0, v24 offset:40960
	ds_write_b32 v0, v25 offset:43008
	ds_write_b32 v0, v26 offset:45056
	ds_write_b32 v0, v27 offset:47104
	ds_write_b32 v0, v28 offset:49152
	ds_write_b32 v0, v29 offset:51200
	ds_write_b32 v0, v30 offset:53248
	ds_write_b32 v0, v31 offset:55296
	ds_write_b32 v0, v32 offset:57344
	ds_write_b32 v0, v33 offset:59392
	ds_write_b32 v0, v34 offset:61440
